# per-workgroup scratch split sized to each workgroup's largest blocks, stored-score loop prefetches four groups ahead
# speedup vs baseline: 1.0354x; 1.0024x over previous
.LBB0_1297:
	v_readlane_b32 s14, v254, 48
	v_readlane_b32 s15, v254, 49
	s_andn2_b64 vcc, exec, s[14:15]
	s_cbranch_vccnz .LBB0_1558
	s_waitcnt lgkmcnt(0)
	s_add_u32 s22, s20, 0x2c200000
	s_addc_u32 s23, s21, 0
	s_add_u32 s18, s20, 0x3f700000
	s_addc_u32 s19, s21, 0
	s_add_u32 s24, s20, 0x2c400000
	s_addc_u32 s25, s21, 0
	s_add_u32 s26, s20, 0x2b200000
	v_readlane_b32 s14, v255, 0
	s_addc_u32 s27, s21, 0
	s_mov_b32 s76, s14
	s_lshr_b32 s32, s14, 1
	s_sub_i32 s100, 316, s32
	s_add_i32 s101, s32, -1
	s_mul_i32 s101, s101, s32
	s_bitcmp1_b32 s14, 0
	s_cselect_b32 s32, s32, 0
	s_add_i32 s101, s101, s32
	s_mul_i32 s32, s14, 317
	s_sub_i32 s101, s32, s101
	s_lshl_b32 s101, s101, 11
	s_add_u32 s101, s101, 0x35d00000
	v_mbcnt_lo_u32_b32 v230, -1, 0
	v_mbcnt_hi_u32_b32 v230, -1, v230
	v_lshlrev_b32_e32 v230, 4, v230
	v_add_u32_e32 v230, s101, v230
	v_readlane_b32 s15, v255, 1
	s_branch .LBB0_1300

.LBB0_1302:
	s_and_b64 s[14:15], s[28:29], exec
	s_cselect_b32 s14, s77, s76
	s_lshl_b32 s34, s14, 4
	s_mov_b32 s14, s33
	s_nop 0
	v_lshl_or_b32 v72, s14, 6, v195
	s_nop 0
	v_readfirstlane_b32 s14, v72
	s_ashr_i32 s30, s14, 6
	s_and_b32 s14, s34, 0xffffffc0
	s_add_i32 s14, s14, 64
	s_ashr_i32 s82, s14, 5
	v_and_b32_e32 v126, 63, v72
	v_and_b32_e32 v125, 15, v72
	s_cmpk_gt_i32 s14, 0x100
	s_mov_b64 s[14:15], -1
	s_cbranch_scc0 .LBB0_1545
	v_or_b32_e32 v0, s34, v125
	v_ashrrev_i32_e32 v1, 31, v0
	v_lshlrev_b64 v[2:3], 10, v[0:1]
	v_lshl_add_u64 v[2:3], s[26:27], 0, v[2:3]
	v_and_b32_e32 v176, 48, v126
	v_lshlrev_b64 v[0:1], 5, v[0:1]
	v_lshl_add_u64 v[68:69], v[2:3], 0, v[176:177]
	v_lshl_add_u64 v[12:13], s[24:25], 0, v[0:1]
	global_load_dwordx4 v[0:3], v[68:69], off
	global_load_dwordx4 v[4:7], v[68:69], off offset:64
	global_load_dwordx4 v[8:11], v[12:13], off offset:16
	s_nop 0
	global_load_dwordx4 v[12:15], v[12:13], off
	s_nop 0
	global_load_dwordx4 v[16:19], v[68:69], off offset:128
	global_load_dwordx4 v[20:23], v[68:69], off offset:192
	global_load_dwordx4 v[24:27], v[68:69], off offset:256
	global_load_dwordx4 v[28:31], v[68:69], off offset:320
	global_load_dwordx4 v[32:35], v[68:69], off offset:384
	global_load_dwordx4 v[36:39], v[68:69], off offset:448
	global_load_dwordx4 v[40:43], v[68:69], off offset:512
	global_load_dwordx4 v[44:47], v[68:69], off offset:576
	global_load_dwordx4 v[48:51], v[68:69], off offset:640
	global_load_dwordx4 v[52:55], v[68:69], off offset:704
	global_load_dwordx4 v[56:59], v[68:69], off offset:768
	global_load_dwordx4 v[60:63], v[68:69], off offset:832
	global_load_dwordx4 v[64:67], v[68:69], off offset:896
	s_nop 0
	global_load_dwordx4 v[68:71], v[68:69], off offset:960
	s_mov_b32 s74, s73
	s_mov_b32 s75, s73
	v_lshlrev_b32_e32 v73, 4, v72
	s_mov_b32 s72, s73
	v_mov_b64_e32 v[76:77], s[74:75]
	v_add_u32_e32 v122, 0, v73
	v_mov_b64_e32 v[74:75], s[72:73]
	v_cmp_gt_i32_e32 vcc, 17, v72
	s_waitcnt vmcnt(0)
	s_barrier
	ds_write_b128 v122, v[74:77]
	ds_write_b128 v122, v[74:77] offset:8192
	ds_write_b128 v122, v[74:77] offset:16384
	ds_write_b128 v122, v[74:77] offset:24576
	ds_write_b128 v122, v[74:77] offset:32768
	ds_write_b128 v122, v[74:77] offset:40960
	ds_write_b128 v122, v[74:77] offset:49152
	ds_write_b128 v122, v[74:77] offset:57344
	s_and_saveexec_b64 s[14:15], vcc
	v_lshl_add_u32 v72, v72, 2, s3
	ds_write_b32 v72, v177 offset:192
	s_or_b64 exec, exec, s[14:15]
	s_lshl_b32 s83, s30, 5
	v_or_b32_e32 v72, s83, v125
	v_lshrrev_b32_e32 v127, 4, v126
	v_ashrrev_i32_e32 v73, 31, v72
	v_lshlrev_b32_e32 v74, 3, v127
	v_mul_u32_u24_e32 v229, 0x70, v125
	v_lshlrev_b64 v[72:73], 7, v[72:73]
	v_sub_u32_e32 v72, v72, v229
	v_lshl_add_u64 v[72:73], s[22:23], 0, v[72:73]
	v_lshlrev_b32_e32 v176, 5, v74
	v_lshl_add_u64 v[72:73], v[72:73], 0, v[176:177]
	s_waitcnt lgkmcnt(0)
	s_barrier
	global_load_dwordx4 v[100:103], v[72:73], off
	global_load_dwordx4 v[96:99], v[72:73], off offset:1024
	global_load_dwordx4 v[92:95], v[72:73], off offset:2048
	global_load_dwordx4 v[88:91], v[72:73], off offset:3072
	s_cmp_lt_i32 s30, s82
	v_lshl_add_u32 v128, v125, 12, 0
	s_cselect_b64 s[36:37], -1, 0
	s_cmp_ge_i32 s30, s82
	v_lshl_add_u64 v[120:121], s[22:23], 0, v[176:177]
	s_cbranch_scc1 .LBB0_1310
	s_waitcnt vmcnt(0)
	v_mov_b64_e32 v[106:107], v[90:91]
	s_add_i32 s14, s82, -1
	s_mov_b32 s15, s30
	v_mov_b64_e32 v[104:105], v[88:89]
	v_mov_b32_e32 v116, v100
	v_mov_b32_e32 v117, v101
	v_mov_b32_e32 v118, v102
	v_mov_b32_e32 v119, v103
	v_mov_b32_e32 v108, v96
	v_mov_b32_e32 v109, v97
	v_mov_b32_e32 v110, v98
	v_mov_b32_e32 v111, v99
	v_mov_b32_e32 v112, v92
	v_mov_b32_e32 v113, v93
	v_mov_b32_e32 v114, v94
	v_mov_b32_e32 v115, v95
	v_lshl_add_u32 v232, s100, 11, v230
	s_branch .LBB0_1308

.LBB0_1308:
	s_waitcnt vmcnt(5)
	v_mfma_f32_16x16x32_bf16 v[130:133], v[116:119], v[0:3], 0
	s_min_i32 s32, s15, s100
	v_lshl_add_u32 v231, s32, 11, v230
	s_add_i32 s31, s15, 8
	s_min_i32 s35, s31, s14
	v_lshl_or_b32 v72, s35, 5, v125
	s_waitcnt vmcnt(3)
	v_mfma_f32_16x16x32_bf16 v[134:137], v[112:115], v[0:3], 0
	v_ashrrev_i32_e32 v73, 31, v72
	v_lshlrev_b64 v[72:73], 7, v[72:73]
	v_sub_u32_e32 v72, v72, v229
	v_lshl_add_u64 v[84:85], v[120:121], 0, v[72:73]
	v_mfma_f32_16x16x32_bf16 v[138:141], v[108:111], v[4:7], v[130:133]
	global_load_dwordx4 v[72:75], v[84:85], off
	global_load_dwordx4 v[76:79], v[84:85], off offset:1024
	global_load_dwordx4 v[80:83], v[84:85], off offset:2048
	s_nop 0
	global_load_dwordx4 v[84:87], v[84:85], off offset:3072
	global_store_dwordx4 v232, v[156:159], s[20:21]
	global_store_dwordx4 v232, v[160:163], s[20:21] offset:1024
	s_nop 1
	v_mov_b32_e32 v156, 0
	s_add_i32 s15, s15, 16
	s_waitcnt vmcnt(8)
	v_mfma_f32_16x16x32_bf16 v[132:135], v[104:107], v[4:7], v[134:137]
	v_max_i32_e32 v123, 0, v138
	v_fmac_f32_e32 v156, v12, v123
	v_mov_b32_e32 v160, 0
	s_min_i32 s35, s15, s14
	s_cmp_ge_i32 s31, s82
	s_nop 3
	v_max_i32_e32 v124, 0, v132
	v_fmac_f32_e32 v160, v12, v124
	v_max_i32_e32 v124, 0, v139
	v_mov_b32_e32 v157, 0
	v_fmac_f32_e32 v157, v12, v124
	v_max_i32_e32 v129, 0, v133
	v_mov_b32_e32 v161, 0
	v_fmac_f32_e32 v161, v12, v129
	v_max_i32_e32 v129, 0, v140
	v_mov_b32_e32 v158, 0
	v_fmac_f32_e32 v158, v12, v129
	v_max_i32_e32 v130, 0, v134
	v_mov_b32_e32 v162, 0
	v_mfma_f32_16x16x32_bf16 v[136:139], v[116:119], v[16:19], 0
	v_fmac_f32_e32 v162, v12, v130
	v_max_i32_e32 v130, 0, v141
	v_mov_b32_e32 v159, 0
	v_mfma_f32_16x16x32_bf16 v[140:143], v[112:115], v[16:19], 0
	v_fmac_f32_e32 v159, v12, v130
	v_max_i32_e32 v135, 0, v135
	v_mov_b32_e32 v163, 0
	v_mfma_f32_16x16x32_bf16 v[136:139], v[108:111], v[20:23], v[136:139]
	v_fmac_f32_e32 v163, v12, v135
	v_mfma_f32_16x16x32_bf16 v[140:143], v[104:107], v[20:23], v[140:143]
	s_nop 6
	v_max_i32_e32 v135, 0, v136
	v_fmac_f32_e32 v156, v13, v135
	v_max_i32_e32 v135, 0, v140
	v_fmac_f32_e32 v160, v13, v135
	v_max_i32_e32 v135, 0, v137
	v_fmac_f32_e32 v157, v13, v135
	v_max_i32_e32 v135, 0, v141
	v_fmac_f32_e32 v161, v13, v135
	v_max_i32_e32 v135, 0, v138
	v_fmac_f32_e32 v158, v13, v135
	v_max_i32_e32 v135, 0, v142
	v_fmac_f32_e32 v162, v13, v135
	v_max_i32_e32 v135, 0, v139
	v_mfma_f32_16x16x32_bf16 v[136:139], v[116:119], v[24:27], 0
	v_fmac_f32_e32 v159, v13, v135
	v_max_i32_e32 v135, 0, v143
	v_fmac_f32_e32 v163, v13, v135
	v_mfma_f32_16x16x32_bf16 v[140:143], v[112:115], v[24:27], 0
	v_mfma_f32_16x16x32_bf16 v[136:139], v[108:111], v[28:31], v[136:139]
	v_mfma_f32_16x16x32_bf16 v[140:143], v[104:107], v[28:31], v[140:143]
	s_nop 6
	v_max_i32_e32 v135, 0, v136
	v_fmac_f32_e32 v156, v14, v135
	v_max_i32_e32 v135, 0, v140
	v_fmac_f32_e32 v160, v14, v135
	v_max_i32_e32 v135, 0, v137
	v_fmac_f32_e32 v157, v14, v135
	v_max_i32_e32 v135, 0, v141
	v_fmac_f32_e32 v161, v14, v135
	v_max_i32_e32 v135, 0, v138
	v_fmac_f32_e32 v158, v14, v135
	v_max_i32_e32 v135, 0, v142
	v_fmac_f32_e32 v162, v14, v135
	v_max_i32_e32 v135, 0, v139
	v_mfma_f32_16x16x32_bf16 v[136:139], v[116:119], v[32:35], 0
	v_fmac_f32_e32 v159, v14, v135
	v_max_i32_e32 v135, 0, v143
	v_fmac_f32_e32 v163, v14, v135
	v_mfma_f32_16x16x32_bf16 v[140:143], v[112:115], v[32:35], 0
	v_mfma_f32_16x16x32_bf16 v[136:139], v[108:111], v[36:39], v[136:139]
	v_mfma_f32_16x16x32_bf16 v[140:143], v[104:107], v[36:39], v[140:143]
	s_nop 6
	v_max_i32_e32 v135, 0, v136
	v_fmac_f32_e32 v156, v15, v135
	v_max_i32_e32 v135, 0, v140
	v_fmac_f32_e32 v160, v15, v135
	v_max_i32_e32 v135, 0, v137
	v_fmac_f32_e32 v157, v15, v135
	v_max_i32_e32 v135, 0, v141
	v_fmac_f32_e32 v161, v15, v135
	v_max_i32_e32 v135, 0, v138
	v_fmac_f32_e32 v158, v15, v135
	v_max_i32_e32 v135, 0, v142
	v_fmac_f32_e32 v162, v15, v135
	v_max_i32_e32 v135, 0, v139
	v_mfma_f32_16x16x32_bf16 v[136:139], v[116:119], v[40:43], 0
	v_fmac_f32_e32 v159, v15, v135
	v_max_i32_e32 v135, 0, v143
	v_fmac_f32_e32 v163, v15, v135
	v_mfma_f32_16x16x32_bf16 v[140:143], v[112:115], v[40:43], 0
	v_mfma_f32_16x16x32_bf16 v[136:139], v[108:111], v[44:47], v[136:139]
	v_mfma_f32_16x16x32_bf16 v[140:143], v[104:107], v[44:47], v[140:143]
	s_nop 6
	v_max_i32_e32 v135, 0, v136
	v_fmac_f32_e32 v156, v8, v135
	v_max_i32_e32 v135, 0, v140
	v_fmac_f32_e32 v160, v8, v135
	v_max_i32_e32 v135, 0, v137
	v_fmac_f32_e32 v157, v8, v135
	v_max_i32_e32 v135, 0, v141
	v_fmac_f32_e32 v161, v8, v135
	v_max_i32_e32 v135, 0, v138
	v_fmac_f32_e32 v158, v8, v135
	v_max_i32_e32 v135, 0, v142
	v_fmac_f32_e32 v162, v8, v135
	v_max_i32_e32 v135, 0, v139
	v_mfma_f32_16x16x32_bf16 v[136:139], v[116:119], v[48:51], 0
	v_fmac_f32_e32 v159, v8, v135
	v_max_i32_e32 v135, 0, v143
	v_fmac_f32_e32 v163, v8, v135
	v_mfma_f32_16x16x32_bf16 v[140:143], v[112:115], v[48:51], 0
	v_mfma_f32_16x16x32_bf16 v[136:139], v[108:111], v[52:55], v[136:139]
	v_mfma_f32_16x16x32_bf16 v[140:143], v[104:107], v[52:55], v[140:143]
	s_nop 6
	v_max_i32_e32 v135, 0, v136
	v_fmac_f32_e32 v156, v9, v135
	v_max_i32_e32 v135, 0, v140
	v_fmac_f32_e32 v160, v9, v135
	v_max_i32_e32 v135, 0, v137
	v_fmac_f32_e32 v157, v9, v135
	v_max_i32_e32 v135, 0, v141
	v_fmac_f32_e32 v161, v9, v135
	v_max_i32_e32 v135, 0, v138
	v_fmac_f32_e32 v158, v9, v135
	v_max_i32_e32 v135, 0, v142
	v_fmac_f32_e32 v162, v9, v135
	v_max_i32_e32 v135, 0, v139
	v_mfma_f32_16x16x32_bf16 v[136:139], v[116:119], v[56:59], 0
	v_fmac_f32_e32 v159, v9, v135
	v_max_i32_e32 v135, 0, v143
	v_fmac_f32_e32 v163, v9, v135
	v_mfma_f32_16x16x32_bf16 v[140:143], v[112:115], v[56:59], 0
	v_mfma_f32_16x16x32_bf16 v[112:115], v[112:115], v[64:67], 0
	v_mfma_f32_16x16x32_bf16 v[116:119], v[116:119], v[64:67], 0
	v_mfma_f32_16x16x32_bf16 v[136:139], v[108:111], v[60:63], v[136:139]
	v_mfma_f32_16x16x32_bf16 v[140:143], v[104:107], v[60:63], v[140:143]
	v_mfma_f32_16x16x32_bf16 v[104:107], v[104:107], v[68:71], v[112:115]
	s_nop 5
	v_max_i32_e32 v135, 0, v136
	v_fmac_f32_e32 v156, v10, v135
	v_max_i32_e32 v135, 0, v140
	v_mfma_f32_16x16x32_bf16 v[108:111], v[108:111], v[68:71], v[116:119]
	v_fmac_f32_e32 v160, v10, v135
	v_max_i32_e32 v104, 0, v104
	v_max_i32_e32 v135, 0, v137
	v_fmac_f32_e32 v157, v10, v135
	v_fmac_f32_e32 v160, v11, v104
	s_nop 5
	v_max_i32_e32 v104, 0, v109
	v_max_i32_e32 v135, 0, v141
	v_fmac_f32_e32 v161, v10, v135
	v_fmac_f32_e32 v157, v11, v104
	v_max_i32_e32 v104, 0, v105
	v_max_i32_e32 v135, 0, v138
	v_fmac_f32_e32 v158, v10, v135
	v_fmac_f32_e32 v161, v11, v104
	v_max_i32_e32 v104, 0, v110
	v_max_i32_e32 v135, 0, v142
	v_fmac_f32_e32 v162, v10, v135
	v_fmac_f32_e32 v158, v11, v104
	v_max_i32_e32 v104, 0, v106
	v_max_i32_e32 v135, 0, v139
	v_fmac_f32_e32 v159, v10, v135
	v_fmac_f32_e32 v162, v11, v104
	v_max_i32_e32 v104, 0, v111
	v_max_i32_e32 v135, 0, v143
	v_fmac_f32_e32 v163, v10, v135
	v_fmac_f32_e32 v159, v11, v104
	v_max_i32_e32 v104, 0, v107
	v_max_i32_e32 v108, 0, v108
	v_fmac_f32_e32 v156, v11, v108
	v_fmac_f32_e32 v163, v11, v104
	s_nop 0
	v_lshrrev_b32 v104, 22, v156
	v_bfe_u32 v105, v156, 21, 1
	v_lshl_add_u32 v104, v104, 2, v128
	v_mad_u32_u24 v105, v105, s1, 1
	ds_add_u32 v104, v105
	v_lshrrev_b32 v104, 22, v157
	v_bfe_u32 v105, v157, 21, 1
	v_lshl_add_u32 v104, v104, 2, v128
	v_mad_u32_u24 v105, v105, s1, 1
	ds_add_u32 v104, v105
	v_lshrrev_b32 v104, 22, v158
	v_bfe_u32 v105, v158, 21, 1
	v_lshl_add_u32 v104, v104, 2, v128
	v_mad_u32_u24 v105, v105, s1, 1
	ds_add_u32 v104, v105
	v_lshrrev_b32 v104, 22, v159
	v_bfe_u32 v105, v159, 21, 1
	v_lshl_add_u32 v104, v104, 2, v128
	v_mad_u32_u24 v105, v105, s1, 1
	ds_add_u32 v104, v105
	v_lshrrev_b32 v104, 22, v160
	v_bfe_u32 v105, v160, 21, 1
	v_lshl_add_u32 v104, v104, 2, v128
	v_mad_u32_u24 v105, v105, s1, 1
	ds_add_u32 v104, v105
	v_lshrrev_b32 v104, 22, v161
	v_bfe_u32 v105, v161, 21, 1
	v_lshl_add_u32 v104, v104, 2, v128
	v_mad_u32_u24 v105, v105, s1, 1
	ds_add_u32 v104, v105
	v_lshrrev_b32 v104, 22, v162
	v_bfe_u32 v105, v162, 21, 1
	v_lshl_add_u32 v104, v104, 2, v128
	v_mad_u32_u24 v105, v105, s1, 1
	ds_add_u32 v104, v105
	v_lshrrev_b32 v104, 22, v163
	v_bfe_u32 v105, v163, 21, 1
	v_lshl_add_u32 v104, v104, 2, v128
	v_mad_u32_u24 v105, v105, s1, 1
	ds_add_u32 v104, v105
	v_lshl_or_b32 v104, s35, 5, v125
	v_ashrrev_i32_e32 v105, 31, v104
	v_lshlrev_b64 v[104:105], 7, v[104:105]
	v_sub_u32_e32 v104, v104, v229
	v_lshl_add_u64 v[104:105], v[120:121], 0, v[104:105]
	global_load_dwordx4 v[116:119], v[104:105], off
	global_load_dwordx4 v[108:111], v[104:105], off offset:1024
	global_load_dwordx4 v[112:115], v[104:105], off offset:2048
	s_nop 0
	global_load_dwordx4 v[104:107], v[104:105], off offset:3072
	global_store_dwordx4 v231, v[156:159], s[20:21]
	global_store_dwordx4 v231, v[160:163], s[20:21] offset:1024
	s_cbranch_scc1 .LBB0_1307
	s_waitcnt vmcnt(11)
	v_mfma_f32_16x16x32_bf16 v[130:133], v[72:75], v[0:3], 0
	s_min_i32 s32, s31, s100
	v_lshl_add_u32 v232, s32, 11, v230
	s_waitcnt vmcnt(9)
	v_mfma_f32_16x16x32_bf16 v[134:137], v[80:83], v[0:3], 0
	v_mfma_f32_16x16x32_bf16 v[138:141], v[76:79], v[4:7], v[130:133]
	s_waitcnt vmcnt(8)
	v_mfma_f32_16x16x32_bf16 v[132:135], v[84:87], v[4:7], v[134:137]
	s_nop 2
	v_mov_b32_e32 v156, 0
	s_nop 1
	v_max_i32_e32 v123, 0, v138
	v_fmac_f32_e32 v156, v12, v123
	v_mov_b32_e32 v160, 0
	v_max_i32_e32 v124, 0, v132
	v_fmac_f32_e32 v160, v12, v124
	v_max_i32_e32 v124, 0, v139
	v_mov_b32_e32 v157, 0
	v_fmac_f32_e32 v157, v12, v124
	v_max_i32_e32 v129, 0, v133
	v_mov_b32_e32 v161, 0
	v_fmac_f32_e32 v161, v12, v129
	v_max_i32_e32 v129, 0, v140
	v_mov_b32_e32 v158, 0
	v_fmac_f32_e32 v158, v12, v129
	v_max_i32_e32 v130, 0, v134
	v_mov_b32_e32 v162, 0
	v_mfma_f32_16x16x32_bf16 v[136:139], v[72:75], v[16:19], 0
	v_fmac_f32_e32 v162, v12, v130
	v_max_i32_e32 v130, 0, v141
	v_mov_b32_e32 v159, 0
	v_mfma_f32_16x16x32_bf16 v[140:143], v[80:83], v[16:19], 0
	v_fmac_f32_e32 v159, v12, v130
	v_max_i32_e32 v135, 0, v135
	v_mov_b32_e32 v163, 0
	v_mfma_f32_16x16x32_bf16 v[136:139], v[76:79], v[20:23], v[136:139]
	v_fmac_f32_e32 v163, v12, v135
	v_mfma_f32_16x16x32_bf16 v[140:143], v[84:87], v[20:23], v[140:143]
	s_nop 6
	v_max_i32_e32 v135, 0, v136
	v_fmac_f32_e32 v156, v13, v135
	v_max_i32_e32 v135, 0, v140
	v_fmac_f32_e32 v160, v13, v135
	v_max_i32_e32 v135, 0, v137
	v_fmac_f32_e32 v157, v13, v135
	v_max_i32_e32 v135, 0, v141
	v_fmac_f32_e32 v161, v13, v135
	v_max_i32_e32 v135, 0, v138
	v_fmac_f32_e32 v158, v13, v135
	v_max_i32_e32 v135, 0, v142
	v_fmac_f32_e32 v162, v13, v135
	v_max_i32_e32 v135, 0, v139
	v_mfma_f32_16x16x32_bf16 v[136:139], v[72:75], v[24:27], 0
	v_fmac_f32_e32 v159, v13, v135
	v_max_i32_e32 v135, 0, v143
	v_fmac_f32_e32 v163, v13, v135
	v_mfma_f32_16x16x32_bf16 v[140:143], v[80:83], v[24:27], 0
	v_mfma_f32_16x16x32_bf16 v[136:139], v[76:79], v[28:31], v[136:139]
	v_mfma_f32_16x16x32_bf16 v[140:143], v[84:87], v[28:31], v[140:143]
	s_nop 6
	v_max_i32_e32 v135, 0, v136
	v_fmac_f32_e32 v156, v14, v135
	v_max_i32_e32 v135, 0, v140
	v_fmac_f32_e32 v160, v14, v135
	v_max_i32_e32 v135, 0, v137
	v_fmac_f32_e32 v157, v14, v135
	v_max_i32_e32 v135, 0, v141
	v_fmac_f32_e32 v161, v14, v135
	v_max_i32_e32 v135, 0, v138
	v_fmac_f32_e32 v158, v14, v135
	v_max_i32_e32 v135, 0, v142
	v_fmac_f32_e32 v162, v14, v135
	v_max_i32_e32 v135, 0, v139
	v_mfma_f32_16x16x32_bf16 v[136:139], v[72:75], v[32:35], 0
	v_fmac_f32_e32 v159, v14, v135
	v_max_i32_e32 v135, 0, v143
	v_fmac_f32_e32 v163, v14, v135
	v_mfma_f32_16x16x32_bf16 v[140:143], v[80:83], v[32:35], 0
	v_mfma_f32_16x16x32_bf16 v[136:139], v[76:79], v[36:39], v[136:139]
	v_mfma_f32_16x16x32_bf16 v[140:143], v[84:87], v[36:39], v[140:143]
	s_nop 6
	v_max_i32_e32 v135, 0, v136
	v_fmac_f32_e32 v156, v15, v135
	v_max_i32_e32 v135, 0, v140
	v_fmac_f32_e32 v160, v15, v135
	v_max_i32_e32 v135, 0, v137
	v_fmac_f32_e32 v157, v15, v135
	v_max_i32_e32 v135, 0, v141
	v_fmac_f32_e32 v161, v15, v135
	v_max_i32_e32 v135, 0, v138
	v_fmac_f32_e32 v158, v15, v135
	v_max_i32_e32 v135, 0, v142
	v_fmac_f32_e32 v162, v15, v135
	v_max_i32_e32 v135, 0, v139
	v_mfma_f32_16x16x32_bf16 v[136:139], v[72:75], v[40:43], 0
	v_fmac_f32_e32 v159, v15, v135
	v_max_i32_e32 v135, 0, v143
	v_fmac_f32_e32 v163, v15, v135
	v_mfma_f32_16x16x32_bf16 v[140:143], v[80:83], v[40:43], 0
	v_mfma_f32_16x16x32_bf16 v[136:139], v[76:79], v[44:47], v[136:139]
	v_mfma_f32_16x16x32_bf16 v[140:143], v[84:87], v[44:47], v[140:143]
	s_nop 6
	v_max_i32_e32 v135, 0, v136
	v_fmac_f32_e32 v156, v8, v135
	v_max_i32_e32 v135, 0, v140
	v_fmac_f32_e32 v160, v8, v135
	v_max_i32_e32 v135, 0, v137
	v_fmac_f32_e32 v157, v8, v135
	v_max_i32_e32 v135, 0, v141
	v_fmac_f32_e32 v161, v8, v135
	v_max_i32_e32 v135, 0, v138
	v_fmac_f32_e32 v158, v8, v135
	v_max_i32_e32 v135, 0, v142
	v_fmac_f32_e32 v162, v8, v135
	v_max_i32_e32 v135, 0, v139
	v_mfma_f32_16x16x32_bf16 v[136:139], v[72:75], v[48:51], 0
	v_fmac_f32_e32 v159, v8, v135
	v_max_i32_e32 v135, 0, v143
	v_fmac_f32_e32 v163, v8, v135
	v_mfma_f32_16x16x32_bf16 v[140:143], v[80:83], v[48:51], 0
	v_mfma_f32_16x16x32_bf16 v[136:139], v[76:79], v[52:55], v[136:139]
	v_mfma_f32_16x16x32_bf16 v[140:143], v[84:87], v[52:55], v[140:143]
	s_nop 6
	v_max_i32_e32 v135, 0, v136
	v_fmac_f32_e32 v156, v9, v135
	v_max_i32_e32 v135, 0, v140
	v_fmac_f32_e32 v160, v9, v135
	v_max_i32_e32 v135, 0, v137
	v_fmac_f32_e32 v157, v9, v135
	v_max_i32_e32 v135, 0, v141
	v_fmac_f32_e32 v161, v9, v135
	v_max_i32_e32 v135, 0, v138
	v_fmac_f32_e32 v158, v9, v135
	v_max_i32_e32 v135, 0, v142
	v_fmac_f32_e32 v162, v9, v135
	v_max_i32_e32 v135, 0, v139
	v_mfma_f32_16x16x32_bf16 v[136:139], v[72:75], v[56:59], 0
	v_fmac_f32_e32 v159, v9, v135
	v_max_i32_e32 v135, 0, v143
	v_fmac_f32_e32 v163, v9, v135
	v_mfma_f32_16x16x32_bf16 v[140:143], v[80:83], v[56:59], 0
	v_mfma_f32_16x16x32_bf16 v[136:139], v[76:79], v[60:63], v[136:139]
	v_mfma_f32_16x16x32_bf16 v[140:143], v[84:87], v[60:63], v[140:143]
	s_nop 6
	v_max_i32_e32 v135, 0, v136
	v_fmac_f32_e32 v156, v10, v135
	v_max_i32_e32 v135, 0, v140
	v_fmac_f32_e32 v160, v10, v135
	v_max_i32_e32 v135, 0, v137
	v_fmac_f32_e32 v157, v10, v135
	v_max_i32_e32 v135, 0, v141
	v_fmac_f32_e32 v161, v10, v135
	v_max_i32_e32 v135, 0, v138
	v_fmac_f32_e32 v158, v10, v135
	v_max_i32_e32 v135, 0, v142
	v_fmac_f32_e32 v162, v10, v135
	v_max_i32_e32 v135, 0, v139
	v_mfma_f32_16x16x32_bf16 v[136:139], v[72:75], v[64:67], 0
	v_fmac_f32_e32 v159, v10, v135
	v_max_i32_e32 v135, 0, v143
	v_fmac_f32_e32 v163, v10, v135
	v_mfma_f32_16x16x32_bf16 v[140:143], v[80:83], v[64:67], 0
	v_mfma_f32_16x16x32_bf16 v[136:139], v[76:79], v[68:71], v[136:139]
	v_mfma_f32_16x16x32_bf16 v[140:143], v[84:87], v[68:71], v[140:143]
	s_nop 6
	v_max_i32_e32 v135, 0, v136
	v_fmac_f32_e32 v156, v11, v135
	v_max_i32_e32 v135, 0, v140
	v_fmac_f32_e32 v160, v11, v135
	v_max_i32_e32 v135, 0, v137
	v_fmac_f32_e32 v157, v11, v135
	v_max_i32_e32 v135, 0, v141
	v_fmac_f32_e32 v161, v11, v135
	v_max_i32_e32 v135, 0, v138
	v_fmac_f32_e32 v158, v11, v135
	v_max_i32_e32 v135, 0, v142
	v_fmac_f32_e32 v162, v11, v135
	v_max_i32_e32 v135, 0, v139
	v_fmac_f32_e32 v159, v11, v135
	v_max_i32_e32 v135, 0, v143
	v_fmac_f32_e32 v163, v11, v135
	v_lshrrev_b32 v135, 22, v156
	v_bfe_u32 v131, v156, 21, 1
	v_mad_u32_u24 v131, v131, s1, 1
	v_lshl_add_u32 v135, v135, 2, v128
	ds_add_u32 v135, v131
	v_lshrrev_b32 v131, 22, v157
	v_bfe_u32 v132, v157, 21, 1
	v_lshl_add_u32 v131, v131, 2, v128
	v_mad_u32_u24 v132, v132, s1, 1
	ds_add_u32 v131, v132
	v_lshrrev_b32 v131, 22, v158
	v_bfe_u32 v132, v158, 21, 1
	v_lshl_add_u32 v131, v131, 2, v128
	v_mad_u32_u24 v132, v132, s1, 1
	ds_add_u32 v131, v132
	v_lshrrev_b32 v131, 22, v159
	v_bfe_u32 v132, v159, 21, 1
	v_lshl_add_u32 v131, v131, 2, v128
	v_mad_u32_u24 v132, v132, s1, 1
	ds_add_u32 v131, v132
	v_lshrrev_b32 v131, 22, v160
	v_bfe_u32 v123, v160, 21, 1
	v_mad_u32_u24 v123, v123, s1, 1
	v_lshl_add_u32 v131, v131, 2, v128
	ds_add_u32 v131, v123
	v_lshrrev_b32 v123, 22, v161
	v_bfe_u32 v124, v161, 21, 1
	v_lshl_add_u32 v123, v123, 2, v128
	v_mad_u32_u24 v124, v124, s1, 1
	ds_add_u32 v123, v124
	v_lshrrev_b32 v123, 22, v162
	v_bfe_u32 v124, v162, 21, 1
	v_lshl_add_u32 v123, v123, 2, v128
	v_mad_u32_u24 v124, v124, s1, 1
	ds_add_u32 v123, v124
	v_lshrrev_b32 v123, 22, v163
	v_bfe_u32 v124, v163, 21, 1
	v_lshl_add_u32 v123, v123, 2, v128
	v_mad_u32_u24 v124, v124, s1, 1
	ds_add_u32 v123, v124
	s_cmp_ge_i32 s15, s82
	s_cbranch_scc0 .LBB0_1308
	global_store_dwordx4 v232, v[156:159], s[20:21]
	global_store_dwordx4 v232, v[160:163], s[20:21] offset:1024
	s_branch .LBB0_1310

.Lpb2_entry:
	s_waitcnt vmcnt(0)
	s_min_i32 s32, s82, s100
	v_mov_b32_e32 v235, 0xffff
	v_ashrrev_i32_e32 v196, 31, v139
	v_lshl_add_u32 v234, s100, 11, v230
	v_lshl_add_u32 v233, s31, 11, v230
	global_load_dwordx4 v[156:159], v233, s[20:21]
	global_load_dwordx4 v[160:163], v233, s[20:21] offset:1024
	global_store_dword v234, v193, s[20:21]
	s_add_i32 s85, s31, 8
	s_min_i32 s85, s85, s100
	v_lshl_add_u32 v233, s85, 11, v230
	global_load_dwordx4 v[178:181], v233, s[20:21]
	global_load_dwordx4 v[182:185], v233, s[20:21] offset:1024
	global_store_dword v234, v193, s[20:21]
	s_add_i32 s85, s31, 16
	s_min_i32 s85, s85, s100
	v_lshl_add_u32 v233, s85, 11, v230
	global_load_dwordx4 v[236:239], v233, s[20:21]
	global_load_dwordx4 v[240:243], v233, s[20:21] offset:1024
	global_store_dword v234, v193, s[20:21]
	s_add_i32 s85, s31, 24
	s_min_i32 s85, s85, s100
	v_lshl_add_u32 v233, s85, 11, v230
	global_load_dwordx4 v[244:247], v233, s[20:21]
	global_load_dwordx4 v[248:251], v233, s[20:21] offset:1024
	global_store_dword v234, v193, s[20:21]
.Lpb2_i0:
	s_add_i32 s85, s31, 32
	s_min_i32 s85, s85, s100
	v_lshl_add_u32 v233, s85, 11, v230
	global_load_dwordx4 v[164:167], v233, s[20:21]
	global_load_dwordx4 v[186:189], v233, s[20:21] offset:1024
	s_waitcnt vmcnt(12)
	v_cmp_ge_f32_e64 s[66:67], v156, v140
	v_cmp_ge_f32_e64 s[50:51], v156, v139
	v_cmp_ge_f32_e32 vcc, v157, v140
	v_cmp_ge_f32_e64 s[52:53], v157, v139
	v_cndmask_b32_e64 v224, 0, 1, s[66:67]
	v_cndmask_b32_e64 v225, 0, 2, vcc
	s_andn2_b64 s[50:51], s[50:51], s[66:67]
	s_andn2_b64 s[52:53], s[52:53], vcc
	v_or_b32_e32 v228, v224, v225
	v_cmp_ge_f32_e64 s[66:67], v158, v140
	v_cmp_ge_f32_e64 s[54:55], v158, v139
	v_cmp_ge_f32_e32 vcc, v159, v140
	v_cmp_ge_f32_e64 s[56:57], v159, v139
	v_cndmask_b32_e64 v224, 0, 4, s[66:67]
	v_cndmask_b32_e64 v225, 0, 8, vcc
	s_andn2_b64 s[54:55], s[54:55], s[66:67]
	s_andn2_b64 s[56:57], s[56:57], vcc
	v_or3_b32 v228, v228, v224, v225
	v_cmp_ge_f32_e64 s[66:67], v160, v140
	v_cmp_ge_f32_e64 s[58:59], v160, v139
	v_cmp_ge_f32_e32 vcc, v161, v140
	v_cmp_ge_f32_e64 s[60:61], v161, v139
	v_cndmask_b32_e64 v224, 0, v201, s[66:67]
	v_cndmask_b32_e64 v225, 0, v200, vcc
	s_andn2_b64 s[58:59], s[58:59], s[66:67]
	s_andn2_b64 s[60:61], s[60:61], vcc
	v_or3_b32 v228, v228, v224, v225
	v_cmp_ge_f32_e64 s[66:67], v162, v140
	v_cmp_ge_f32_e64 s[62:63], v162, v139
	v_cmp_ge_f32_e32 vcc, v163, v140
	v_cmp_ge_f32_e64 s[64:65], v163, v139
	v_cndmask_b32_e64 v224, 0, v199, s[66:67]
	v_cndmask_b32_e64 v225, 0, v198, vcc
	s_andn2_b64 s[62:63], s[62:63], s[66:67]
	s_andn2_b64 s[64:65], s[64:65], vcc
	v_or3_b32 v228, v228, v224, v225
	v_lshlrev_b32_e32 v104, v143, v228
	ds_bpermute_b32 v105, v144, v104
	v_mov_b32_e32 v227, s96
	s_mov_b64 s[14:15], exec
	s_mov_b64 exec, s[50:51]
	ds_add_rtn_u32 v214, v142, v193
	s_mov_b64 exec, s[52:53]
	ds_add_rtn_u32 v215, v142, v193
	s_mov_b64 exec, s[54:55]
	ds_add_rtn_u32 v216, v142, v193
	s_mov_b64 exec, s[56:57]
	ds_add_rtn_u32 v217, v142, v193
	s_mov_b64 exec, s[58:59]
	ds_add_rtn_u32 v218, v142, v193
	s_mov_b64 exec, s[60:61]
	ds_add_rtn_u32 v219, v142, v193
	s_mov_b64 exec, s[62:63]
	ds_add_rtn_u32 v220, v142, v193
	s_mov_b64 exec, s[64:65]
	ds_add_rtn_u32 v221, v142, v193
	s_mov_b64 exec, s[50:51]
	v_xor_b32_e32 v206, v196, v156
	v_bfe_u32 v222, v206, 11, 10
	v_bfe_u32 v223, v206, 10, 1
	v_lshl_add_u32 v222, v222, 2, v128
	v_mad_u32_u24 v223, v223, v235, 1
	ds_add_u32 v222, v223
	s_mov_b64 exec, s[52:53]
	v_xor_b32_e32 v207, v196, v157
	v_bfe_u32 v222, v207, 11, 10
	v_bfe_u32 v223, v207, 10, 1
	v_lshl_add_u32 v222, v222, 2, v128
	v_mad_u32_u24 v223, v223, v235, 1
	ds_add_u32 v222, v223
	s_mov_b64 exec, s[54:55]
	v_xor_b32_e32 v208, v196, v158
	v_bfe_u32 v222, v208, 11, 10
	v_bfe_u32 v223, v208, 10, 1
	v_lshl_add_u32 v222, v222, 2, v128
	v_mad_u32_u24 v223, v223, v235, 1
	ds_add_u32 v222, v223
	s_mov_b64 exec, s[56:57]
	v_xor_b32_e32 v209, v196, v159
	v_bfe_u32 v222, v209, 11, 10
	v_bfe_u32 v223, v209, 10, 1
	v_lshl_add_u32 v222, v222, 2, v128
	v_mad_u32_u24 v223, v223, v235, 1
	ds_add_u32 v222, v223
	s_waitcnt lgkmcnt(8)
	s_mov_b64 exec, s[58:59]
	v_xor_b32_e32 v210, v196, v160
	v_bfe_u32 v222, v210, 11, 10
	v_bfe_u32 v223, v210, 10, 1
	v_lshl_add_u32 v222, v222, 2, v128
	v_mad_u32_u24 v223, v223, v235, 1
	ds_add_u32 v222, v223
	s_mov_b64 exec, s[60:61]
	v_xor_b32_e32 v211, v196, v161
	v_bfe_u32 v222, v211, 11, 10
	v_bfe_u32 v223, v211, 10, 1
	v_lshl_add_u32 v222, v222, 2, v128
	v_mad_u32_u24 v223, v223, v235, 1
	ds_add_u32 v222, v223
	s_mov_b64 exec, s[62:63]
	v_xor_b32_e32 v212, v196, v162
	v_bfe_u32 v222, v212, 11, 10
	v_bfe_u32 v223, v212, 10, 1
	v_lshl_add_u32 v222, v222, 2, v128
	v_mad_u32_u24 v223, v223, v235, 1
	ds_add_u32 v222, v223
	s_mov_b64 exec, s[64:65]
	v_xor_b32_e32 v213, v196, v163
	v_bfe_u32 v222, v213, 11, 10
	v_bfe_u32 v223, v213, 10, 1
	v_lshl_add_u32 v222, v222, 2, v128
	v_mad_u32_u24 v223, v223, v235, 1
	ds_add_u32 v222, v223
	s_waitcnt lgkmcnt(8)
	s_mov_b64 exec, s[14:15]
	v_or_b32_e32 v104, v105, v104
	ds_bpermute_b32 v105, v145, v104
	s_mov_b64 exec, s[50:51]
	v_cmp_lt_u32_e64 s[66:67], s0, v214
	s_add_i32 s85, s74, 0x0
	v_bfe_u32 v224, v206, 10, 11
	v_lshl_add_u32 v222, v214, 2, v141
	v_add3_u32 v224, v224, v124, s85
	s_andn2_b64 exec, exec, s[66:67]
	ds_write_b32 v222, v224
	s_mov_b64 exec, s[66:67]
	ds_write_b32 v227, v193
	s_mov_b64 exec, s[52:53]
	v_cmp_lt_u32_e64 s[66:67], s0, v215
	s_add_i32 s85, s74, 0x800
	v_bfe_u32 v224, v207, 10, 11
	v_lshl_add_u32 v222, v215, 2, v141
	v_add3_u32 v224, v224, v124, s85
	s_andn2_b64 exec, exec, s[66:67]
	ds_write_b32 v222, v224
	s_mov_b64 exec, s[66:67]
	ds_write_b32 v227, v193
	s_waitcnt lgkmcnt(8)
	s_mov_b64 exec, s[54:55]
	v_cmp_lt_u32_e64 s[66:67], s0, v216
	s_add_i32 s85, s74, 0x1000
	v_bfe_u32 v224, v208, 10, 11
	v_lshl_add_u32 v222, v216, 2, v141
	v_add3_u32 v224, v224, v124, s85
	s_andn2_b64 exec, exec, s[66:67]
	ds_write_b32 v222, v224
	s_mov_b64 exec, s[66:67]
	ds_write_b32 v227, v193
	s_mov_b64 exec, s[56:57]
	v_cmp_lt_u32_e64 s[66:67], s0, v217
	s_add_i32 s85, s74, 0x1800
	v_bfe_u32 v224, v209, 10, 11
	v_lshl_add_u32 v222, v217, 2, v141
	v_add3_u32 v224, v224, v124, s85
	s_andn2_b64 exec, exec, s[66:67]
	ds_write_b32 v222, v224
	s_mov_b64 exec, s[66:67]
	ds_write_b32 v227, v193
	s_waitcnt lgkmcnt(8)
	s_mov_b64 exec, s[58:59]
	v_cmp_lt_u32_e64 s[66:67], s0, v218
	s_add_i32 s85, s74, 0x8000
	v_bfe_u32 v224, v210, 10, 11
	v_lshl_add_u32 v222, v218, 2, v141
	v_add3_u32 v224, v224, v124, s85
	s_andn2_b64 exec, exec, s[66:67]
	ds_write_b32 v222, v224
	s_mov_b64 exec, s[66:67]
	ds_write_b32 v227, v193
	s_mov_b64 exec, s[60:61]
	v_cmp_lt_u32_e64 s[66:67], s0, v219
	s_add_i32 s85, s74, 0x8800
	v_bfe_u32 v224, v211, 10, 11
	v_lshl_add_u32 v222, v219, 2, v141
	v_add3_u32 v224, v224, v124, s85
	s_andn2_b64 exec, exec, s[66:67]
	ds_write_b32 v222, v224
	s_mov_b64 exec, s[66:67]
	ds_write_b32 v227, v193
	s_waitcnt lgkmcnt(8)
	s_mov_b64 exec, s[62:63]
	v_cmp_lt_u32_e64 s[66:67], s0, v220
	s_add_i32 s85, s74, 0x9000
	v_bfe_u32 v224, v212, 10, 11
	v_lshl_add_u32 v222, v220, 2, v141
	v_add3_u32 v224, v224, v124, s85
	s_andn2_b64 exec, exec, s[66:67]
	ds_write_b32 v222, v224
	s_mov_b64 exec, s[66:67]
	ds_write_b32 v227, v193
	s_mov_b64 exec, s[64:65]
	v_cmp_lt_u32_e64 s[66:67], s0, v221
	s_add_i32 s85, s74, 0x9800
	v_bfe_u32 v224, v213, 10, 11
	v_lshl_add_u32 v222, v221, 2, v141
	v_add3_u32 v224, v224, v124, s85
	s_andn2_b64 exec, exec, s[66:67]
	ds_write_b32 v222, v224
	s_mov_b64 exec, s[66:67]
	ds_write_b32 v227, v193
	s_mov_b64 exec, s[14:15]
	s_and_saveexec_b64 s[14:15], s[38:39]
	v_or_b32_e32 v106, v104, v105
	v_lshl_add_u64 v[104:105], v[122:123], 0, s[74:75]
	v_add_co_u32_e32 v104, vcc, 0x3f700000, v104
	s_nop 1
	v_addc_co_u32_e32 v105, vcc, 0, v105, vcc
	global_store_dword v[104:105], v106, off
	s_or_b64 exec, exec, s[14:15]
	s_add_u32 s74, s74, 0x80000
	s_addc_u32 s75, s75, 0
	s_add_i32 s31, s31, 8
	s_cmp_ge_i32 s31, s32
	s_cbranch_scc1 .Lpb2_done
.Lpb2_i1:
	s_add_i32 s85, s31, 32
	s_min_i32 s85, s85, s100
	v_lshl_add_u32 v233, s85, 11, v230
	global_load_dwordx4 v[156:159], v233, s[20:21]
	global_load_dwordx4 v[160:163], v233, s[20:21] offset:1024
	s_waitcnt vmcnt(12)
	v_cmp_ge_f32_e64 s[66:67], v178, v140
	v_cmp_ge_f32_e64 s[50:51], v178, v139
	v_cmp_ge_f32_e32 vcc, v179, v140
	v_cmp_ge_f32_e64 s[52:53], v179, v139
	v_cndmask_b32_e64 v224, 0, 1, s[66:67]
	v_cndmask_b32_e64 v225, 0, 2, vcc
	s_andn2_b64 s[50:51], s[50:51], s[66:67]
	s_andn2_b64 s[52:53], s[52:53], vcc
	v_or_b32_e32 v228, v224, v225
	v_cmp_ge_f32_e64 s[66:67], v180, v140
	v_cmp_ge_f32_e64 s[54:55], v180, v139
	v_cmp_ge_f32_e32 vcc, v181, v140
	v_cmp_ge_f32_e64 s[56:57], v181, v139
	v_cndmask_b32_e64 v224, 0, 4, s[66:67]
	v_cndmask_b32_e64 v225, 0, 8, vcc
	s_andn2_b64 s[54:55], s[54:55], s[66:67]
	s_andn2_b64 s[56:57], s[56:57], vcc
	v_or3_b32 v228, v228, v224, v225
	v_cmp_ge_f32_e64 s[66:67], v182, v140
	v_cmp_ge_f32_e64 s[58:59], v182, v139
	v_cmp_ge_f32_e32 vcc, v183, v140
	v_cmp_ge_f32_e64 s[60:61], v183, v139
	v_cndmask_b32_e64 v224, 0, v201, s[66:67]
	v_cndmask_b32_e64 v225, 0, v200, vcc
	s_andn2_b64 s[58:59], s[58:59], s[66:67]
	s_andn2_b64 s[60:61], s[60:61], vcc
	v_or3_b32 v228, v228, v224, v225
	v_cmp_ge_f32_e64 s[66:67], v184, v140
	v_cmp_ge_f32_e64 s[62:63], v184, v139
	v_cmp_ge_f32_e32 vcc, v185, v140
	v_cmp_ge_f32_e64 s[64:65], v185, v139
	v_cndmask_b32_e64 v224, 0, v199, s[66:67]
	v_cndmask_b32_e64 v225, 0, v198, vcc
	s_andn2_b64 s[62:63], s[62:63], s[66:67]
	s_andn2_b64 s[64:65], s[64:65], vcc
	v_or3_b32 v228, v228, v224, v225
	v_lshlrev_b32_e32 v104, v143, v228
	ds_bpermute_b32 v105, v144, v104
	v_mov_b32_e32 v227, s96
	s_mov_b64 s[14:15], exec
	s_mov_b64 exec, s[50:51]
	ds_add_rtn_u32 v214, v142, v193
	s_mov_b64 exec, s[52:53]
	ds_add_rtn_u32 v215, v142, v193
	s_mov_b64 exec, s[54:55]
	ds_add_rtn_u32 v216, v142, v193
	s_mov_b64 exec, s[56:57]
	ds_add_rtn_u32 v217, v142, v193
	s_mov_b64 exec, s[58:59]
	ds_add_rtn_u32 v218, v142, v193
	s_mov_b64 exec, s[60:61]
	ds_add_rtn_u32 v219, v142, v193
	s_mov_b64 exec, s[62:63]
	ds_add_rtn_u32 v220, v142, v193
	s_mov_b64 exec, s[64:65]
	ds_add_rtn_u32 v221, v142, v193
	s_mov_b64 exec, s[50:51]
	v_xor_b32_e32 v206, v196, v178
	v_bfe_u32 v222, v206, 11, 10
	v_bfe_u32 v223, v206, 10, 1
	v_lshl_add_u32 v222, v222, 2, v128
	v_mad_u32_u24 v223, v223, v235, 1
	ds_add_u32 v222, v223
	s_mov_b64 exec, s[52:53]
	v_xor_b32_e32 v207, v196, v179
	v_bfe_u32 v222, v207, 11, 10
	v_bfe_u32 v223, v207, 10, 1
	v_lshl_add_u32 v222, v222, 2, v128
	v_mad_u32_u24 v223, v223, v235, 1
	ds_add_u32 v222, v223
	s_mov_b64 exec, s[54:55]
	v_xor_b32_e32 v208, v196, v180
	v_bfe_u32 v222, v208, 11, 10
	v_bfe_u32 v223, v208, 10, 1
	v_lshl_add_u32 v222, v222, 2, v128
	v_mad_u32_u24 v223, v223, v235, 1
	ds_add_u32 v222, v223
	s_mov_b64 exec, s[56:57]
	v_xor_b32_e32 v209, v196, v181
	v_bfe_u32 v222, v209, 11, 10
	v_bfe_u32 v223, v209, 10, 1
	v_lshl_add_u32 v222, v222, 2, v128
	v_mad_u32_u24 v223, v223, v235, 1
	ds_add_u32 v222, v223
	s_waitcnt lgkmcnt(8)
	s_mov_b64 exec, s[58:59]
	v_xor_b32_e32 v210, v196, v182
	v_bfe_u32 v222, v210, 11, 10
	v_bfe_u32 v223, v210, 10, 1
	v_lshl_add_u32 v222, v222, 2, v128
	v_mad_u32_u24 v223, v223, v235, 1
	ds_add_u32 v222, v223
	s_mov_b64 exec, s[60:61]
	v_xor_b32_e32 v211, v196, v183
	v_bfe_u32 v222, v211, 11, 10
	v_bfe_u32 v223, v211, 10, 1
	v_lshl_add_u32 v222, v222, 2, v128
	v_mad_u32_u24 v223, v223, v235, 1
	ds_add_u32 v222, v223
	s_mov_b64 exec, s[62:63]
	v_xor_b32_e32 v212, v196, v184
	v_bfe_u32 v222, v212, 11, 10
	v_bfe_u32 v223, v212, 10, 1
	v_lshl_add_u32 v222, v222, 2, v128
	v_mad_u32_u24 v223, v223, v235, 1
	ds_add_u32 v222, v223
	s_mov_b64 exec, s[64:65]
	v_xor_b32_e32 v213, v196, v185
	v_bfe_u32 v222, v213, 11, 10
	v_bfe_u32 v223, v213, 10, 1
	v_lshl_add_u32 v222, v222, 2, v128
	v_mad_u32_u24 v223, v223, v235, 1
	ds_add_u32 v222, v223
	s_waitcnt lgkmcnt(8)
	s_mov_b64 exec, s[14:15]
	v_or_b32_e32 v104, v105, v104
	ds_bpermute_b32 v105, v145, v104
	s_mov_b64 exec, s[50:51]
	v_cmp_lt_u32_e64 s[66:67], s0, v214
	s_add_i32 s85, s74, 0x0
	v_bfe_u32 v224, v206, 10, 11
	v_lshl_add_u32 v222, v214, 2, v141
	v_add3_u32 v224, v224, v124, s85
	s_andn2_b64 exec, exec, s[66:67]
	ds_write_b32 v222, v224
	s_mov_b64 exec, s[66:67]
	ds_write_b32 v227, v193
	s_mov_b64 exec, s[52:53]
	v_cmp_lt_u32_e64 s[66:67], s0, v215
	s_add_i32 s85, s74, 0x800
	v_bfe_u32 v224, v207, 10, 11
	v_lshl_add_u32 v222, v215, 2, v141
	v_add3_u32 v224, v224, v124, s85
	s_andn2_b64 exec, exec, s[66:67]
	ds_write_b32 v222, v224
	s_mov_b64 exec, s[66:67]
	ds_write_b32 v227, v193
	s_waitcnt lgkmcnt(8)
	s_mov_b64 exec, s[54:55]
	v_cmp_lt_u32_e64 s[66:67], s0, v216
	s_add_i32 s85, s74, 0x1000
	v_bfe_u32 v224, v208, 10, 11
	v_lshl_add_u32 v222, v216, 2, v141
	v_add3_u32 v224, v224, v124, s85
	s_andn2_b64 exec, exec, s[66:67]
	ds_write_b32 v222, v224
	s_mov_b64 exec, s[66:67]
	ds_write_b32 v227, v193
	s_mov_b64 exec, s[56:57]
	v_cmp_lt_u32_e64 s[66:67], s0, v217
	s_add_i32 s85, s74, 0x1800
	v_bfe_u32 v224, v209, 10, 11
	v_lshl_add_u32 v222, v217, 2, v141
	v_add3_u32 v224, v224, v124, s85
	s_andn2_b64 exec, exec, s[66:67]
	ds_write_b32 v222, v224
	s_mov_b64 exec, s[66:67]
	ds_write_b32 v227, v193
	s_waitcnt lgkmcnt(8)
	s_mov_b64 exec, s[58:59]
	v_cmp_lt_u32_e64 s[66:67], s0, v218
	s_add_i32 s85, s74, 0x8000
	v_bfe_u32 v224, v210, 10, 11
	v_lshl_add_u32 v222, v218, 2, v141
	v_add3_u32 v224, v224, v124, s85
	s_andn2_b64 exec, exec, s[66:67]
	ds_write_b32 v222, v224
	s_mov_b64 exec, s[66:67]
	ds_write_b32 v227, v193
	s_mov_b64 exec, s[60:61]
	v_cmp_lt_u32_e64 s[66:67], s0, v219
	s_add_i32 s85, s74, 0x8800
	v_bfe_u32 v224, v211, 10, 11
	v_lshl_add_u32 v222, v219, 2, v141
	v_add3_u32 v224, v224, v124, s85
	s_andn2_b64 exec, exec, s[66:67]
	ds_write_b32 v222, v224
	s_mov_b64 exec, s[66:67]
	ds_write_b32 v227, v193
	s_waitcnt lgkmcnt(8)
	s_mov_b64 exec, s[62:63]
	v_cmp_lt_u32_e64 s[66:67], s0, v220
	s_add_i32 s85, s74, 0x9000
	v_bfe_u32 v224, v212, 10, 11
	v_lshl_add_u32 v222, v220, 2, v141
	v_add3_u32 v224, v224, v124, s85
	s_andn2_b64 exec, exec, s[66:67]
	ds_write_b32 v222, v224
	s_mov_b64 exec, s[66:67]
	ds_write_b32 v227, v193
	s_mov_b64 exec, s[64:65]
	v_cmp_lt_u32_e64 s[66:67], s0, v221
	s_add_i32 s85, s74, 0x9800
	v_bfe_u32 v224, v213, 10, 11
	v_lshl_add_u32 v222, v221, 2, v141
	v_add3_u32 v224, v224, v124, s85
	s_andn2_b64 exec, exec, s[66:67]
	ds_write_b32 v222, v224
	s_mov_b64 exec, s[66:67]
	ds_write_b32 v227, v193
	s_mov_b64 exec, s[14:15]
	s_and_saveexec_b64 s[14:15], s[38:39]
	v_or_b32_e32 v106, v104, v105
	v_lshl_add_u64 v[104:105], v[122:123], 0, s[74:75]
	v_add_co_u32_e32 v104, vcc, 0x3f700000, v104
	s_nop 1
	v_addc_co_u32_e32 v105, vcc, 0, v105, vcc
	global_store_dword v[104:105], v106, off
	s_or_b64 exec, exec, s[14:15]
	s_add_u32 s74, s74, 0x80000
	s_addc_u32 s75, s75, 0
	s_add_i32 s31, s31, 8
	s_cmp_ge_i32 s31, s32
	s_cbranch_scc1 .Lpb2_done
.Lpb2_i2:
	s_add_i32 s85, s31, 32
	s_min_i32 s85, s85, s100
	v_lshl_add_u32 v233, s85, 11, v230
	global_load_dwordx4 v[178:181], v233, s[20:21]
	global_load_dwordx4 v[182:185], v233, s[20:21] offset:1024
	s_waitcnt vmcnt(12)
	v_cmp_ge_f32_e64 s[66:67], v236, v140
	v_cmp_ge_f32_e64 s[50:51], v236, v139
	v_cmp_ge_f32_e32 vcc, v237, v140
	v_cmp_ge_f32_e64 s[52:53], v237, v139
	v_cndmask_b32_e64 v224, 0, 1, s[66:67]
	v_cndmask_b32_e64 v225, 0, 2, vcc
	s_andn2_b64 s[50:51], s[50:51], s[66:67]
	s_andn2_b64 s[52:53], s[52:53], vcc
	v_or_b32_e32 v228, v224, v225
	v_cmp_ge_f32_e64 s[66:67], v238, v140
	v_cmp_ge_f32_e64 s[54:55], v238, v139
	v_cmp_ge_f32_e32 vcc, v239, v140
	v_cmp_ge_f32_e64 s[56:57], v239, v139
	v_cndmask_b32_e64 v224, 0, 4, s[66:67]
	v_cndmask_b32_e64 v225, 0, 8, vcc
	s_andn2_b64 s[54:55], s[54:55], s[66:67]
	s_andn2_b64 s[56:57], s[56:57], vcc
	v_or3_b32 v228, v228, v224, v225
	v_cmp_ge_f32_e64 s[66:67], v240, v140
	v_cmp_ge_f32_e64 s[58:59], v240, v139
	v_cmp_ge_f32_e32 vcc, v241, v140
	v_cmp_ge_f32_e64 s[60:61], v241, v139
	v_cndmask_b32_e64 v224, 0, v201, s[66:67]
	v_cndmask_b32_e64 v225, 0, v200, vcc
	s_andn2_b64 s[58:59], s[58:59], s[66:67]
	s_andn2_b64 s[60:61], s[60:61], vcc
	v_or3_b32 v228, v228, v224, v225
	v_cmp_ge_f32_e64 s[66:67], v242, v140
	v_cmp_ge_f32_e64 s[62:63], v242, v139
	v_cmp_ge_f32_e32 vcc, v243, v140
	v_cmp_ge_f32_e64 s[64:65], v243, v139
	v_cndmask_b32_e64 v224, 0, v199, s[66:67]
	v_cndmask_b32_e64 v225, 0, v198, vcc
	s_andn2_b64 s[62:63], s[62:63], s[66:67]
	s_andn2_b64 s[64:65], s[64:65], vcc
	v_or3_b32 v228, v228, v224, v225
	v_lshlrev_b32_e32 v104, v143, v228
	ds_bpermute_b32 v105, v144, v104
	v_mov_b32_e32 v227, s96
	s_mov_b64 s[14:15], exec
	s_mov_b64 exec, s[50:51]
	ds_add_rtn_u32 v214, v142, v193
	s_mov_b64 exec, s[52:53]
	ds_add_rtn_u32 v215, v142, v193
	s_mov_b64 exec, s[54:55]
	ds_add_rtn_u32 v216, v142, v193
	s_mov_b64 exec, s[56:57]
	ds_add_rtn_u32 v217, v142, v193
	s_mov_b64 exec, s[58:59]
	ds_add_rtn_u32 v218, v142, v193
	s_mov_b64 exec, s[60:61]
	ds_add_rtn_u32 v219, v142, v193
	s_mov_b64 exec, s[62:63]
	ds_add_rtn_u32 v220, v142, v193
	s_mov_b64 exec, s[64:65]
	ds_add_rtn_u32 v221, v142, v193
	s_mov_b64 exec, s[50:51]
	v_xor_b32_e32 v206, v196, v236
	v_bfe_u32 v222, v206, 11, 10
	v_bfe_u32 v223, v206, 10, 1
	v_lshl_add_u32 v222, v222, 2, v128
	v_mad_u32_u24 v223, v223, v235, 1
	ds_add_u32 v222, v223
	s_mov_b64 exec, s[52:53]
	v_xor_b32_e32 v207, v196, v237
	v_bfe_u32 v222, v207, 11, 10
	v_bfe_u32 v223, v207, 10, 1
	v_lshl_add_u32 v222, v222, 2, v128
	v_mad_u32_u24 v223, v223, v235, 1
	ds_add_u32 v222, v223
	s_mov_b64 exec, s[54:55]
	v_xor_b32_e32 v208, v196, v238
	v_bfe_u32 v222, v208, 11, 10
	v_bfe_u32 v223, v208, 10, 1
	v_lshl_add_u32 v222, v222, 2, v128
	v_mad_u32_u24 v223, v223, v235, 1
	ds_add_u32 v222, v223
	s_mov_b64 exec, s[56:57]
	v_xor_b32_e32 v209, v196, v239
	v_bfe_u32 v222, v209, 11, 10
	v_bfe_u32 v223, v209, 10, 1
	v_lshl_add_u32 v222, v222, 2, v128
	v_mad_u32_u24 v223, v223, v235, 1
	ds_add_u32 v222, v223
	s_waitcnt lgkmcnt(8)
	s_mov_b64 exec, s[58:59]
	v_xor_b32_e32 v210, v196, v240
	v_bfe_u32 v222, v210, 11, 10
	v_bfe_u32 v223, v210, 10, 1
	v_lshl_add_u32 v222, v222, 2, v128
	v_mad_u32_u24 v223, v223, v235, 1
	ds_add_u32 v222, v223
	s_mov_b64 exec, s[60:61]
	v_xor_b32_e32 v211, v196, v241
	v_bfe_u32 v222, v211, 11, 10
	v_bfe_u32 v223, v211, 10, 1
	v_lshl_add_u32 v222, v222, 2, v128
	v_mad_u32_u24 v223, v223, v235, 1
	ds_add_u32 v222, v223
	s_mov_b64 exec, s[62:63]
	v_xor_b32_e32 v212, v196, v242
	v_bfe_u32 v222, v212, 11, 10
	v_bfe_u32 v223, v212, 10, 1
	v_lshl_add_u32 v222, v222, 2, v128
	v_mad_u32_u24 v223, v223, v235, 1
	ds_add_u32 v222, v223
	s_mov_b64 exec, s[64:65]
	v_xor_b32_e32 v213, v196, v243
	v_bfe_u32 v222, v213, 11, 10
	v_bfe_u32 v223, v213, 10, 1
	v_lshl_add_u32 v222, v222, 2, v128
	v_mad_u32_u24 v223, v223, v235, 1
	ds_add_u32 v222, v223
	s_waitcnt lgkmcnt(8)
	s_mov_b64 exec, s[14:15]
	v_or_b32_e32 v104, v105, v104
	ds_bpermute_b32 v105, v145, v104
	s_mov_b64 exec, s[50:51]
	v_cmp_lt_u32_e64 s[66:67], s0, v214
	s_add_i32 s85, s74, 0x0
	v_bfe_u32 v224, v206, 10, 11
	v_lshl_add_u32 v222, v214, 2, v141
	v_add3_u32 v224, v224, v124, s85
	s_andn2_b64 exec, exec, s[66:67]
	ds_write_b32 v222, v224
	s_mov_b64 exec, s[66:67]
	ds_write_b32 v227, v193
	s_mov_b64 exec, s[52:53]
	v_cmp_lt_u32_e64 s[66:67], s0, v215
	s_add_i32 s85, s74, 0x800
	v_bfe_u32 v224, v207, 10, 11
	v_lshl_add_u32 v222, v215, 2, v141
	v_add3_u32 v224, v224, v124, s85
	s_andn2_b64 exec, exec, s[66:67]
	ds_write_b32 v222, v224
	s_mov_b64 exec, s[66:67]
	ds_write_b32 v227, v193
	s_waitcnt lgkmcnt(8)
	s_mov_b64 exec, s[54:55]
	v_cmp_lt_u32_e64 s[66:67], s0, v216
	s_add_i32 s85, s74, 0x1000
	v_bfe_u32 v224, v208, 10, 11
	v_lshl_add_u32 v222, v216, 2, v141
	v_add3_u32 v224, v224, v124, s85
	s_andn2_b64 exec, exec, s[66:67]
	ds_write_b32 v222, v224
	s_mov_b64 exec, s[66:67]
	ds_write_b32 v227, v193
	s_mov_b64 exec, s[56:57]
	v_cmp_lt_u32_e64 s[66:67], s0, v217
	s_add_i32 s85, s74, 0x1800
	v_bfe_u32 v224, v209, 10, 11
	v_lshl_add_u32 v222, v217, 2, v141
	v_add3_u32 v224, v224, v124, s85
	s_andn2_b64 exec, exec, s[66:67]
	ds_write_b32 v222, v224
	s_mov_b64 exec, s[66:67]
	ds_write_b32 v227, v193
	s_waitcnt lgkmcnt(8)
	s_mov_b64 exec, s[58:59]
	v_cmp_lt_u32_e64 s[66:67], s0, v218
	s_add_i32 s85, s74, 0x8000
	v_bfe_u32 v224, v210, 10, 11
	v_lshl_add_u32 v222, v218, 2, v141
	v_add3_u32 v224, v224, v124, s85
	s_andn2_b64 exec, exec, s[66:67]
	ds_write_b32 v222, v224
	s_mov_b64 exec, s[66:67]
	ds_write_b32 v227, v193
	s_mov_b64 exec, s[60:61]
	v_cmp_lt_u32_e64 s[66:67], s0, v219
	s_add_i32 s85, s74, 0x8800
	v_bfe_u32 v224, v211, 10, 11
	v_lshl_add_u32 v222, v219, 2, v141
	v_add3_u32 v224, v224, v124, s85
	s_andn2_b64 exec, exec, s[66:67]
	ds_write_b32 v222, v224
	s_mov_b64 exec, s[66:67]
	ds_write_b32 v227, v193
	s_waitcnt lgkmcnt(8)
	s_mov_b64 exec, s[62:63]
	v_cmp_lt_u32_e64 s[66:67], s0, v220
	s_add_i32 s85, s74, 0x9000
	v_bfe_u32 v224, v212, 10, 11
	v_lshl_add_u32 v222, v220, 2, v141
	v_add3_u32 v224, v224, v124, s85
	s_andn2_b64 exec, exec, s[66:67]
	ds_write_b32 v222, v224
	s_mov_b64 exec, s[66:67]
	ds_write_b32 v227, v193
	s_mov_b64 exec, s[64:65]
	v_cmp_lt_u32_e64 s[66:67], s0, v221
	s_add_i32 s85, s74, 0x9800
	v_bfe_u32 v224, v213, 10, 11
	v_lshl_add_u32 v222, v221, 2, v141
	v_add3_u32 v224, v224, v124, s85
	s_andn2_b64 exec, exec, s[66:67]
	ds_write_b32 v222, v224
	s_mov_b64 exec, s[66:67]
	ds_write_b32 v227, v193
	s_mov_b64 exec, s[14:15]
	s_and_saveexec_b64 s[14:15], s[38:39]
	v_or_b32_e32 v106, v104, v105
	v_lshl_add_u64 v[104:105], v[122:123], 0, s[74:75]
	v_add_co_u32_e32 v104, vcc, 0x3f700000, v104
	s_nop 1
	v_addc_co_u32_e32 v105, vcc, 0, v105, vcc
	global_store_dword v[104:105], v106, off
	s_or_b64 exec, exec, s[14:15]
	s_add_u32 s74, s74, 0x80000
	s_addc_u32 s75, s75, 0
	s_add_i32 s31, s31, 8
	s_cmp_ge_i32 s31, s32
	s_cbranch_scc1 .Lpb2_done
.Lpb2_i3:
	s_add_i32 s85, s31, 32
	s_min_i32 s85, s85, s100
	v_lshl_add_u32 v233, s85, 11, v230
	global_load_dwordx4 v[236:239], v233, s[20:21]
	global_load_dwordx4 v[240:243], v233, s[20:21] offset:1024
	s_waitcnt vmcnt(12)
	v_cmp_ge_f32_e64 s[66:67], v244, v140
	v_cmp_ge_f32_e64 s[50:51], v244, v139
	v_cmp_ge_f32_e32 vcc, v245, v140
	v_cmp_ge_f32_e64 s[52:53], v245, v139
	v_cndmask_b32_e64 v224, 0, 1, s[66:67]
	v_cndmask_b32_e64 v225, 0, 2, vcc
	s_andn2_b64 s[50:51], s[50:51], s[66:67]
	s_andn2_b64 s[52:53], s[52:53], vcc
	v_or_b32_e32 v228, v224, v225
	v_cmp_ge_f32_e64 s[66:67], v246, v140
	v_cmp_ge_f32_e64 s[54:55], v246, v139
	v_cmp_ge_f32_e32 vcc, v247, v140
	v_cmp_ge_f32_e64 s[56:57], v247, v139
	v_cndmask_b32_e64 v224, 0, 4, s[66:67]
	v_cndmask_b32_e64 v225, 0, 8, vcc
	s_andn2_b64 s[54:55], s[54:55], s[66:67]
	s_andn2_b64 s[56:57], s[56:57], vcc
	v_or3_b32 v228, v228, v224, v225
	v_cmp_ge_f32_e64 s[66:67], v248, v140
	v_cmp_ge_f32_e64 s[58:59], v248, v139
	v_cmp_ge_f32_e32 vcc, v249, v140
	v_cmp_ge_f32_e64 s[60:61], v249, v139
	v_cndmask_b32_e64 v224, 0, v201, s[66:67]
	v_cndmask_b32_e64 v225, 0, v200, vcc
	s_andn2_b64 s[58:59], s[58:59], s[66:67]
	s_andn2_b64 s[60:61], s[60:61], vcc
	v_or3_b32 v228, v228, v224, v225
	v_cmp_ge_f32_e64 s[66:67], v250, v140
	v_cmp_ge_f32_e64 s[62:63], v250, v139
	v_cmp_ge_f32_e32 vcc, v251, v140
	v_cmp_ge_f32_e64 s[64:65], v251, v139
	v_cndmask_b32_e64 v224, 0, v199, s[66:67]
	v_cndmask_b32_e64 v225, 0, v198, vcc
	s_andn2_b64 s[62:63], s[62:63], s[66:67]
	s_andn2_b64 s[64:65], s[64:65], vcc
	v_or3_b32 v228, v228, v224, v225
	v_lshlrev_b32_e32 v104, v143, v228
	ds_bpermute_b32 v105, v144, v104
	v_mov_b32_e32 v227, s96
	s_mov_b64 s[14:15], exec
	s_mov_b64 exec, s[50:51]
	ds_add_rtn_u32 v214, v142, v193
	s_mov_b64 exec, s[52:53]
	ds_add_rtn_u32 v215, v142, v193
	s_mov_b64 exec, s[54:55]
	ds_add_rtn_u32 v216, v142, v193
	s_mov_b64 exec, s[56:57]
	ds_add_rtn_u32 v217, v142, v193
	s_mov_b64 exec, s[58:59]
	ds_add_rtn_u32 v218, v142, v193
	s_mov_b64 exec, s[60:61]
	ds_add_rtn_u32 v219, v142, v193
	s_mov_b64 exec, s[62:63]
	ds_add_rtn_u32 v220, v142, v193
	s_mov_b64 exec, s[64:65]
	ds_add_rtn_u32 v221, v142, v193
	s_mov_b64 exec, s[50:51]
	v_xor_b32_e32 v206, v196, v244
	v_bfe_u32 v222, v206, 11, 10
	v_bfe_u32 v223, v206, 10, 1
	v_lshl_add_u32 v222, v222, 2, v128
	v_mad_u32_u24 v223, v223, v235, 1
	ds_add_u32 v222, v223
	s_mov_b64 exec, s[52:53]
	v_xor_b32_e32 v207, v196, v245
	v_bfe_u32 v222, v207, 11, 10
	v_bfe_u32 v223, v207, 10, 1
	v_lshl_add_u32 v222, v222, 2, v128
	v_mad_u32_u24 v223, v223, v235, 1
	ds_add_u32 v222, v223
	s_mov_b64 exec, s[54:55]
	v_xor_b32_e32 v208, v196, v246
	v_bfe_u32 v222, v208, 11, 10
	v_bfe_u32 v223, v208, 10, 1
	v_lshl_add_u32 v222, v222, 2, v128
	v_mad_u32_u24 v223, v223, v235, 1
	ds_add_u32 v222, v223
	s_mov_b64 exec, s[56:57]
	v_xor_b32_e32 v209, v196, v247
	v_bfe_u32 v222, v209, 11, 10
	v_bfe_u32 v223, v209, 10, 1
	v_lshl_add_u32 v222, v222, 2, v128
	v_mad_u32_u24 v223, v223, v235, 1
	ds_add_u32 v222, v223
	s_waitcnt lgkmcnt(8)
	s_mov_b64 exec, s[58:59]
	v_xor_b32_e32 v210, v196, v248
	v_bfe_u32 v222, v210, 11, 10
	v_bfe_u32 v223, v210, 10, 1
	v_lshl_add_u32 v222, v222, 2, v128
	v_mad_u32_u24 v223, v223, v235, 1
	ds_add_u32 v222, v223
	s_mov_b64 exec, s[60:61]
	v_xor_b32_e32 v211, v196, v249
	v_bfe_u32 v222, v211, 11, 10
	v_bfe_u32 v223, v211, 10, 1
	v_lshl_add_u32 v222, v222, 2, v128
	v_mad_u32_u24 v223, v223, v235, 1
	ds_add_u32 v222, v223
	s_mov_b64 exec, s[62:63]
	v_xor_b32_e32 v212, v196, v250
	v_bfe_u32 v222, v212, 11, 10
	v_bfe_u32 v223, v212, 10, 1
	v_lshl_add_u32 v222, v222, 2, v128
	v_mad_u32_u24 v223, v223, v235, 1
	ds_add_u32 v222, v223
	s_mov_b64 exec, s[64:65]
	v_xor_b32_e32 v213, v196, v251
	v_bfe_u32 v222, v213, 11, 10
	v_bfe_u32 v223, v213, 10, 1
	v_lshl_add_u32 v222, v222, 2, v128
	v_mad_u32_u24 v223, v223, v235, 1
	ds_add_u32 v222, v223
	s_waitcnt lgkmcnt(8)
	s_mov_b64 exec, s[14:15]
	v_or_b32_e32 v104, v105, v104
	ds_bpermute_b32 v105, v145, v104
	s_mov_b64 exec, s[50:51]
	v_cmp_lt_u32_e64 s[66:67], s0, v214
	s_add_i32 s85, s74, 0x0
	v_bfe_u32 v224, v206, 10, 11
	v_lshl_add_u32 v222, v214, 2, v141
	v_add3_u32 v224, v224, v124, s85
	s_andn2_b64 exec, exec, s[66:67]
	ds_write_b32 v222, v224
	s_mov_b64 exec, s[66:67]
	ds_write_b32 v227, v193
	s_mov_b64 exec, s[52:53]
	v_cmp_lt_u32_e64 s[66:67], s0, v215
	s_add_i32 s85, s74, 0x800
	v_bfe_u32 v224, v207, 10, 11
	v_lshl_add_u32 v222, v215, 2, v141
	v_add3_u32 v224, v224, v124, s85
	s_andn2_b64 exec, exec, s[66:67]
	ds_write_b32 v222, v224
	s_mov_b64 exec, s[66:67]
	ds_write_b32 v227, v193
	s_waitcnt lgkmcnt(8)
	s_mov_b64 exec, s[54:55]
	v_cmp_lt_u32_e64 s[66:67], s0, v216
	s_add_i32 s85, s74, 0x1000
	v_bfe_u32 v224, v208, 10, 11
	v_lshl_add_u32 v222, v216, 2, v141
	v_add3_u32 v224, v224, v124, s85
	s_andn2_b64 exec, exec, s[66:67]
	ds_write_b32 v222, v224
	s_mov_b64 exec, s[66:67]
	ds_write_b32 v227, v193
	s_mov_b64 exec, s[56:57]
	v_cmp_lt_u32_e64 s[66:67], s0, v217
	s_add_i32 s85, s74, 0x1800
	v_bfe_u32 v224, v209, 10, 11
	v_lshl_add_u32 v222, v217, 2, v141
	v_add3_u32 v224, v224, v124, s85
	s_andn2_b64 exec, exec, s[66:67]
	ds_write_b32 v222, v224
	s_mov_b64 exec, s[66:67]
	ds_write_b32 v227, v193
	s_waitcnt lgkmcnt(8)
	s_mov_b64 exec, s[58:59]
	v_cmp_lt_u32_e64 s[66:67], s0, v218
	s_add_i32 s85, s74, 0x8000
	v_bfe_u32 v224, v210, 10, 11
	v_lshl_add_u32 v222, v218, 2, v141
	v_add3_u32 v224, v224, v124, s85
	s_andn2_b64 exec, exec, s[66:67]
	ds_write_b32 v222, v224
	s_mov_b64 exec, s[66:67]
	ds_write_b32 v227, v193
	s_mov_b64 exec, s[60:61]
	v_cmp_lt_u32_e64 s[66:67], s0, v219
	s_add_i32 s85, s74, 0x8800
	v_bfe_u32 v224, v211, 10, 11
	v_lshl_add_u32 v222, v219, 2, v141
	v_add3_u32 v224, v224, v124, s85
	s_andn2_b64 exec, exec, s[66:67]
	ds_write_b32 v222, v224
	s_mov_b64 exec, s[66:67]
	ds_write_b32 v227, v193
	s_waitcnt lgkmcnt(8)
	s_mov_b64 exec, s[62:63]
	v_cmp_lt_u32_e64 s[66:67], s0, v220
	s_add_i32 s85, s74, 0x9000
	v_bfe_u32 v224, v212, 10, 11
	v_lshl_add_u32 v222, v220, 2, v141
	v_add3_u32 v224, v224, v124, s85
	s_andn2_b64 exec, exec, s[66:67]
	ds_write_b32 v222, v224
	s_mov_b64 exec, s[66:67]
	ds_write_b32 v227, v193
	s_mov_b64 exec, s[64:65]
	v_cmp_lt_u32_e64 s[66:67], s0, v221
	s_add_i32 s85, s74, 0x9800
	v_bfe_u32 v224, v213, 10, 11
	v_lshl_add_u32 v222, v221, 2, v141
	v_add3_u32 v224, v224, v124, s85
	s_andn2_b64 exec, exec, s[66:67]
	ds_write_b32 v222, v224
	s_mov_b64 exec, s[66:67]
	ds_write_b32 v227, v193
	s_mov_b64 exec, s[14:15]
	s_and_saveexec_b64 s[14:15], s[38:39]
	v_or_b32_e32 v106, v104, v105
	v_lshl_add_u64 v[104:105], v[122:123], 0, s[74:75]
	v_add_co_u32_e32 v104, vcc, 0x3f700000, v104
	s_nop 1
	v_addc_co_u32_e32 v105, vcc, 0, v105, vcc
	global_store_dword v[104:105], v106, off
	s_or_b64 exec, exec, s[14:15]
	s_add_u32 s74, s74, 0x80000
	s_addc_u32 s75, s75, 0
	s_add_i32 s31, s31, 8
	s_cmp_ge_i32 s31, s32
	s_cbranch_scc1 .Lpb2_done
.Lpb2_i4:
	s_add_i32 s85, s31, 32
	s_min_i32 s85, s85, s100
	v_lshl_add_u32 v233, s85, 11, v230
	global_load_dwordx4 v[244:247], v233, s[20:21]
	global_load_dwordx4 v[248:251], v233, s[20:21] offset:1024
	s_waitcnt vmcnt(12)
	v_cmp_ge_f32_e64 s[66:67], v164, v140
	v_cmp_ge_f32_e64 s[50:51], v164, v139
	v_cmp_ge_f32_e32 vcc, v165, v140
	v_cmp_ge_f32_e64 s[52:53], v165, v139
	v_cndmask_b32_e64 v224, 0, 1, s[66:67]
	v_cndmask_b32_e64 v225, 0, 2, vcc
	s_andn2_b64 s[50:51], s[50:51], s[66:67]
	s_andn2_b64 s[52:53], s[52:53], vcc
	v_or_b32_e32 v228, v224, v225
	v_cmp_ge_f32_e64 s[66:67], v166, v140
	v_cmp_ge_f32_e64 s[54:55], v166, v139
	v_cmp_ge_f32_e32 vcc, v167, v140
	v_cmp_ge_f32_e64 s[56:57], v167, v139
	v_cndmask_b32_e64 v224, 0, 4, s[66:67]
	v_cndmask_b32_e64 v225, 0, 8, vcc
	s_andn2_b64 s[54:55], s[54:55], s[66:67]
	s_andn2_b64 s[56:57], s[56:57], vcc
	v_or3_b32 v228, v228, v224, v225
	v_cmp_ge_f32_e64 s[66:67], v186, v140
	v_cmp_ge_f32_e64 s[58:59], v186, v139
	v_cmp_ge_f32_e32 vcc, v187, v140
	v_cmp_ge_f32_e64 s[60:61], v187, v139
	v_cndmask_b32_e64 v224, 0, v201, s[66:67]
	v_cndmask_b32_e64 v225, 0, v200, vcc
	s_andn2_b64 s[58:59], s[58:59], s[66:67]
	s_andn2_b64 s[60:61], s[60:61], vcc
	v_or3_b32 v228, v228, v224, v225
	v_cmp_ge_f32_e64 s[66:67], v188, v140
	v_cmp_ge_f32_e64 s[62:63], v188, v139
	v_cmp_ge_f32_e32 vcc, v189, v140
	v_cmp_ge_f32_e64 s[64:65], v189, v139
	v_cndmask_b32_e64 v224, 0, v199, s[66:67]
	v_cndmask_b32_e64 v225, 0, v198, vcc
	s_andn2_b64 s[62:63], s[62:63], s[66:67]
	s_andn2_b64 s[64:65], s[64:65], vcc
	v_or3_b32 v228, v228, v224, v225
	v_lshlrev_b32_e32 v104, v143, v228
	ds_bpermute_b32 v105, v144, v104
	v_mov_b32_e32 v227, s96
	s_mov_b64 s[14:15], exec
	s_mov_b64 exec, s[50:51]
	ds_add_rtn_u32 v214, v142, v193
	s_mov_b64 exec, s[52:53]
	ds_add_rtn_u32 v215, v142, v193
	s_mov_b64 exec, s[54:55]
	ds_add_rtn_u32 v216, v142, v193
	s_mov_b64 exec, s[56:57]
	ds_add_rtn_u32 v217, v142, v193
	s_mov_b64 exec, s[58:59]
	ds_add_rtn_u32 v218, v142, v193
	s_mov_b64 exec, s[60:61]
	ds_add_rtn_u32 v219, v142, v193
	s_mov_b64 exec, s[62:63]
	ds_add_rtn_u32 v220, v142, v193
	s_mov_b64 exec, s[64:65]
	ds_add_rtn_u32 v221, v142, v193
	s_mov_b64 exec, s[50:51]
	v_xor_b32_e32 v206, v196, v164
	v_bfe_u32 v222, v206, 11, 10
	v_bfe_u32 v223, v206, 10, 1
	v_lshl_add_u32 v222, v222, 2, v128
	v_mad_u32_u24 v223, v223, v235, 1
	ds_add_u32 v222, v223
	s_mov_b64 exec, s[52:53]
	v_xor_b32_e32 v207, v196, v165
	v_bfe_u32 v222, v207, 11, 10
	v_bfe_u32 v223, v207, 10, 1
	v_lshl_add_u32 v222, v222, 2, v128
	v_mad_u32_u24 v223, v223, v235, 1
	ds_add_u32 v222, v223
	s_mov_b64 exec, s[54:55]
	v_xor_b32_e32 v208, v196, v166
	v_bfe_u32 v222, v208, 11, 10
	v_bfe_u32 v223, v208, 10, 1
	v_lshl_add_u32 v222, v222, 2, v128
	v_mad_u32_u24 v223, v223, v235, 1
	ds_add_u32 v222, v223
	s_mov_b64 exec, s[56:57]
	v_xor_b32_e32 v209, v196, v167
	v_bfe_u32 v222, v209, 11, 10
	v_bfe_u32 v223, v209, 10, 1
	v_lshl_add_u32 v222, v222, 2, v128
	v_mad_u32_u24 v223, v223, v235, 1
	ds_add_u32 v222, v223
	s_waitcnt lgkmcnt(8)
	s_mov_b64 exec, s[58:59]
	v_xor_b32_e32 v210, v196, v186
	v_bfe_u32 v222, v210, 11, 10
	v_bfe_u32 v223, v210, 10, 1
	v_lshl_add_u32 v222, v222, 2, v128
	v_mad_u32_u24 v223, v223, v235, 1
	ds_add_u32 v222, v223
	s_mov_b64 exec, s[60:61]
	v_xor_b32_e32 v211, v196, v187
	v_bfe_u32 v222, v211, 11, 10
	v_bfe_u32 v223, v211, 10, 1
	v_lshl_add_u32 v222, v222, 2, v128
	v_mad_u32_u24 v223, v223, v235, 1
	ds_add_u32 v222, v223
	s_mov_b64 exec, s[62:63]
	v_xor_b32_e32 v212, v196, v188
	v_bfe_u32 v222, v212, 11, 10
	v_bfe_u32 v223, v212, 10, 1
	v_lshl_add_u32 v222, v222, 2, v128
	v_mad_u32_u24 v223, v223, v235, 1
	ds_add_u32 v222, v223
	s_mov_b64 exec, s[64:65]
	v_xor_b32_e32 v213, v196, v189
	v_bfe_u32 v222, v213, 11, 10
	v_bfe_u32 v223, v213, 10, 1
	v_lshl_add_u32 v222, v222, 2, v128
	v_mad_u32_u24 v223, v223, v235, 1
	ds_add_u32 v222, v223
	s_waitcnt lgkmcnt(8)
	s_mov_b64 exec, s[14:15]
	v_or_b32_e32 v104, v105, v104
	ds_bpermute_b32 v105, v145, v104
	s_mov_b64 exec, s[50:51]
	v_cmp_lt_u32_e64 s[66:67], s0, v214
	s_add_i32 s85, s74, 0x0
	v_bfe_u32 v224, v206, 10, 11
	v_lshl_add_u32 v222, v214, 2, v141
	v_add3_u32 v224, v224, v124, s85
	s_andn2_b64 exec, exec, s[66:67]
	ds_write_b32 v222, v224
	s_mov_b64 exec, s[66:67]
	ds_write_b32 v227, v193
	s_mov_b64 exec, s[52:53]
	v_cmp_lt_u32_e64 s[66:67], s0, v215
	s_add_i32 s85, s74, 0x800
	v_bfe_u32 v224, v207, 10, 11
	v_lshl_add_u32 v222, v215, 2, v141
	v_add3_u32 v224, v224, v124, s85
	s_andn2_b64 exec, exec, s[66:67]
	ds_write_b32 v222, v224
	s_mov_b64 exec, s[66:67]
	ds_write_b32 v227, v193
	s_waitcnt lgkmcnt(8)
	s_mov_b64 exec, s[54:55]
	v_cmp_lt_u32_e64 s[66:67], s0, v216
	s_add_i32 s85, s74, 0x1000
	v_bfe_u32 v224, v208, 10, 11
	v_lshl_add_u32 v222, v216, 2, v141
	v_add3_u32 v224, v224, v124, s85
	s_andn2_b64 exec, exec, s[66:67]
	ds_write_b32 v222, v224
	s_mov_b64 exec, s[66:67]
	ds_write_b32 v227, v193
	s_mov_b64 exec, s[56:57]
	v_cmp_lt_u32_e64 s[66:67], s0, v217
	s_add_i32 s85, s74, 0x1800
	v_bfe_u32 v224, v209, 10, 11
	v_lshl_add_u32 v222, v217, 2, v141
	v_add3_u32 v224, v224, v124, s85
	s_andn2_b64 exec, exec, s[66:67]
	ds_write_b32 v222, v224
	s_mov_b64 exec, s[66:67]
	ds_write_b32 v227, v193
	s_waitcnt lgkmcnt(8)
	s_mov_b64 exec, s[58:59]
	v_cmp_lt_u32_e64 s[66:67], s0, v218
	s_add_i32 s85, s74, 0x8000
	v_bfe_u32 v224, v210, 10, 11
	v_lshl_add_u32 v222, v218, 2, v141
	v_add3_u32 v224, v224, v124, s85
	s_andn2_b64 exec, exec, s[66:67]
	ds_write_b32 v222, v224
	s_mov_b64 exec, s[66:67]
	ds_write_b32 v227, v193
	s_mov_b64 exec, s[60:61]
	v_cmp_lt_u32_e64 s[66:67], s0, v219
	s_add_i32 s85, s74, 0x8800
	v_bfe_u32 v224, v211, 10, 11
	v_lshl_add_u32 v222, v219, 2, v141
	v_add3_u32 v224, v224, v124, s85
	s_andn2_b64 exec, exec, s[66:67]
	ds_write_b32 v222, v224
	s_mov_b64 exec, s[66:67]
	ds_write_b32 v227, v193
	s_waitcnt lgkmcnt(8)
	s_mov_b64 exec, s[62:63]
	v_cmp_lt_u32_e64 s[66:67], s0, v220
	s_add_i32 s85, s74, 0x9000
	v_bfe_u32 v224, v212, 10, 11
	v_lshl_add_u32 v222, v220, 2, v141
	v_add3_u32 v224, v224, v124, s85
	s_andn2_b64 exec, exec, s[66:67]
	ds_write_b32 v222, v224
	s_mov_b64 exec, s[66:67]
	ds_write_b32 v227, v193
	s_mov_b64 exec, s[64:65]
	v_cmp_lt_u32_e64 s[66:67], s0, v221
	s_add_i32 s85, s74, 0x9800
	v_bfe_u32 v224, v213, 10, 11
	v_lshl_add_u32 v222, v221, 2, v141
	v_add3_u32 v224, v224, v124, s85
	s_andn2_b64 exec, exec, s[66:67]
	ds_write_b32 v222, v224
	s_mov_b64 exec, s[66:67]
	ds_write_b32 v227, v193
	s_mov_b64 exec, s[14:15]
	s_and_saveexec_b64 s[14:15], s[38:39]
	v_or_b32_e32 v106, v104, v105
	v_lshl_add_u64 v[104:105], v[122:123], 0, s[74:75]
	v_add_co_u32_e32 v104, vcc, 0x3f700000, v104
	s_nop 1
	v_addc_co_u32_e32 v105, vcc, 0, v105, vcc
	global_store_dword v[104:105], v106, off
	s_or_b64 exec, exec, s[14:15]
	s_add_u32 s74, s74, 0x80000
	s_addc_u32 s75, s75, 0
	s_add_i32 s31, s31, 8
	s_cmp_ge_i32 s31, s32
	s_cbranch_scc0 .Lpb2_i0
